# pipelined weight-paced attention + per-tile alternating s_setprio between wave halves (0-3 vs 4-7)
# speedup vs baseline: 1.0057x; 1.0057x over previous
.LBB0_733:
	s_or_b64 exec, exec, s[8:9]
	s_movk_i32 s4, 0xf0
	s_cmp_lg_u32 0, -1
	v_lshlrev_b32_e32 v39, 8, v141
	v_bitop3_b32 v80, v142, s4, v136 bitop3:0x48
	s_cselect_b32 s10, 0, 0
	v_cvt_pk_bf16_f32 v96, v134, v135
	v_cvt_pk_bf16_f32 v97, v132, v133
	v_cvt_pk_bf16_f32 v98, v130, v131
	v_cvt_pk_bf16_f32 v99, v128, v129
	v_cvt_pk_bf16_f32 v100, v126, v127
	v_cvt_pk_bf16_f32 v101, v124, v125
	v_cvt_pk_bf16_f32 v102, v122, v123
	v_cvt_pk_bf16_f32 v103, v120, v121
	v_cvt_pk_bf16_f32 v104, v70, v71
	v_cvt_pk_bf16_f32 v105, v74, v75
	v_cvt_pk_bf16_f32 v106, v64, v65
	v_cvt_pk_bf16_f32 v107, v68, v69
	v_cvt_pk_bf16_f32 v108, v60, v61
	v_cvt_pk_bf16_f32 v109, v66, v67
	v_cvt_pk_bf16_f32 v110, v56, v57
	v_cvt_pk_bf16_f32 v111, v58, v59
	v_cvt_pk_bf16_f32 v112, v112, v113
	v_cvt_pk_bf16_f32 v113, v118, v119
	v_cvt_pk_bf16_f32 v114, v114, v115
	v_cvt_pk_bf16_f32 v115, v116, v117
	v_cvt_pk_bf16_f32 v116, v78, v79
	v_cvt_pk_bf16_f32 v117, v76, v77
	v_cvt_pk_bf16_f32 v118, v72, v73
	v_cvt_pk_bf16_f32 v119, v62, v63
	v_cvt_pk_bf16_f32 v120, v52, v53
	v_cvt_pk_bf16_f32 v121, v54, v55
	v_cvt_pk_bf16_f32 v122, v46, v47
	v_cvt_pk_bf16_f32 v123, v50, v51
	v_cvt_pk_bf16_f32 v124, v44, v45
	v_cvt_pk_bf16_f32 v125, v48, v49
	v_cvt_pk_bf16_f32 v126, v40, v41
	v_cvt_pk_bf16_f32 v127, v42, v43
	v_readlane_b32 s100, v250, 8
	v_mbcnt_lo_u32_b32 v68, -1, 0
	v_mbcnt_hi_u32_b32 v68, -1, v68
	s_nop 1
	v_add_u32_e32 v69, s100, v68
	v_lshrrev_b32_e32 v70, 3, v69
	v_and_b32_e32 v71, 7, v69
	v_lshrrev_b32_e32 v72, 2, v71
	v_bfe_u32 v73, v71, 1, 1
	v_and_b32_e32 v74, 1, v71
	v_lshlrev_b32_e32 v74, 1, v74
	v_lshl_add_u32 v75, v72, 2, v74
	v_bfe_u32 v76, v70, 1, 3
	v_xor_b32_e32 v77, v75, v76
	v_add_u32_e32 v78, 1, v75
	v_xor_b32_e32 v78, v78, v76
	v_lshlrev_b32_e32 v79, 7, v70
	v_lshl_add_u32 v79, v73, 3, v79
	v_lshl_add_u32 v64, v77, 4, v79
	v_lshl_add_u32 v65, v78, 4, v79
	v_add_u32_e32 v66, 0x2000, v64
	v_add_u32_e32 v67, 0x2000, v65
	v_or_b32_e32 v81, v39, v80
	s_add_i32 s15, s10, 0x10000
	v_and_b32_e32 v82, 6, v137
	v_lshrrev_b32_e32 v84, 4, v136
	s_waitcnt vmcnt(0)
	s_waitcnt vmcnt(0)
	s_add_i32 s11, s10, 0x12000
	v_lshl_add_u32 v83, v139, 7, s10
	v_bitop3_b32 v85, v84, v82, 7 bitop3:0x6c
	v_and_b32_e32 v86, 8, v138
	v_or_b32_e32 v82, 1, v82
	v_add_u32_e32 v225, s15, v81
	s_waitcnt vmcnt(4)
	ds_write_b128 v225, v[24:27] offset:0
	v_lshlrev_b32_e32 v85, 4, v85
	v_add_u32_e32 v87, v83, v86
	v_bitop3_b32 v82, v84, v82, 7 bitop3:0x6c
	v_add3_u32 v226, v80, s11, v39
	ds_write_b128 v226, v[28:31] offset:0
	v_lshlrev_b32_e32 v82, 4, v82
	v_add_u32_e32 v227, v87, v85
	ds_write_b64 v64, v[12:13] offset:0
	v_lshrrev_b32_e32 v32, 5, v136
	v_add_u32_e32 v83, 0x2000, v83
	v_or_b32_e32 v84, v85, v86
	v_add_u32_e32 v228, v87, v82
	ds_write_b64 v65, v[14:15] offset:0
	v_xor_b32_e32 v32, v32, v137
	v_or_b32_e32 v86, v82, v86
	v_add_u32_e32 v229, v84, v83
	ds_write_b64 v66, v[4:5] offset:0
	v_lshlrev_b32_e32 v32, 4, v32
	v_add_u32_e32 v184, v86, v83
	ds_write_b64 v67, v[6:7] offset:0
	v_lshlrev_b32_e32 v33, 8, v143
	v_and_b32_e32 v32, 16, v32
	v_bfe_u32 v35, v137, 1, 3
	s_waitcnt vmcnt(4)
	ds_write_b128 v225, v[20:23] offset:0x4000
	v_lshlrev_b32_e32 v36, 5, v35
	v_add3_u32 v32, v33, s15, v32
	s_movk_i32 s16, 0x60
	ds_write_b128 v226, v[16:19] offset:0x4000
	v_xad_u32 v204, v36, s16, v32
	s_movk_i32 s16, 0x80
	ds_write_b64 v64, v[8:9] offset:0x4000
	v_xad_u32 v205, v36, s16, v32
	s_movk_i32 s16, 0xa0
	ds_write_b64 v65, v[10:11] offset:0x4000
	s_add_u32 s8, s6, 0x100
	v_xad_u32 v206, v36, s16, v32
	s_movk_i32 s16, 0xc0
	ds_write_b64 v66, v[0:1] offset:0x4000
	s_addc_u32 s9, s7, 0
	v_xad_u32 v207, v36, s16, v32
	s_movk_i32 s16, 0xe0
	ds_write_b64 v67, v[2:3] offset:0x4000
	v_add_u32_e32 v201, v32, v36
	v_xad_u32 v202, v36, 32, v32
	v_xad_u32 v203, v36, 64, v32
	v_xad_u32 v208, v36, s16, v32
	v_lshl_add_u32 v32, v143, 7, s10
	s_add_u32 s10, s78, 0x20000
	global_load_dwordx4 v[132:135], v198, s[8:9]
	s_addc_u32 s11, s79, 0
	global_load_dwordx4 v[128:131], v199, s[8:9]
	v_lshrrev_b32_e32 v34, 1, v137
	global_load_dwordx4 v[136:139], v196, s[10:11]
	s_add_u32 s6, s6, 0x180
	v_bitop3_b32 v34, v140, v34, 7 bitop3:0x78
	v_bitop3_b32 v37, v140, v35, 2 bitop3:0x36
	v_bitop3_b32 v38, v140, v35, 4 bitop3:0x36
	v_bitop3_b32 v35, v140, v35, 6 bitop3:0x36
	global_load_dwordx4 v[140:143], v197, s[10:11]
	s_addc_u32 s7, s7, 0
	s_add_u32 s8, s78, 0x30000
	global_load_dwordx4 v[148:151], v198, s[6:7]
	s_addc_u32 s9, s79, 0
	global_load_dwordx4 v[144:147], v199, s[6:7]
	global_load_dwordx4 v[152:155], v196, s[8:9]
	s_add_u32 s10, s13, s14
	global_load_dwordx4 v[156:159], v197, s[8:9]
	s_addc_u32 s11, s12, 0
	s_add_u32 s12, s41, s30
	v_mov_b32_e32 v0, 0
	s_mov_b32 s4, 0
	v_lshl_add_u32 v209, v34, 4, v32
	v_lshl_add_u32 v210, v37, 4, v32
	v_lshl_add_u32 v211, v38, 4, v32
	v_lshl_add_u32 v224, v35, 4, v32
	s_addc_u32 s13, 0, s31
	v_mov_b32_e32 v1, v0
	v_mov_b32_e32 v2, v0
	v_mov_b32_e32 v3, v0
	v_mov_b32_e32 v4, v0
	v_mov_b32_e32 v5, v0
	v_mov_b32_e32 v6, v0
	v_mov_b32_e32 v7, v0
	v_mov_b32_e32 v8, v0
	v_mov_b32_e32 v9, v0
	v_mov_b32_e32 v10, v0
	v_mov_b32_e32 v11, v0
	v_mov_b32_e32 v12, v0
	v_mov_b32_e32 v13, v0
	v_mov_b32_e32 v14, v0
	v_mov_b32_e32 v15, v0
	v_mov_b32_e32 v16, v0
	v_mov_b32_e32 v17, v0
	v_mov_b32_e32 v18, v0
	v_mov_b32_e32 v19, v0
	v_mov_b32_e32 v20, v0
	v_mov_b32_e32 v21, v0
	v_mov_b32_e32 v22, v0
	v_mov_b32_e32 v23, v0
	v_mov_b32_e32 v24, v0
	v_mov_b32_e32 v25, v0
	v_mov_b32_e32 v26, v0
	v_mov_b32_e32 v27, v0
	v_mov_b32_e32 v28, v0
	v_mov_b32_e32 v29, v0
	v_mov_b32_e32 v30, v0
	v_mov_b32_e32 v31, v0
	v_mov_b32_e32 v32, v0
	v_mov_b32_e32 v33, v0
	v_mov_b32_e32 v34, v0
	v_mov_b32_e32 v35, v0
	v_mov_b32_e32 v36, v0
	v_mov_b32_e32 v37, v0
	v_mov_b32_e32 v38, v0
	v_mov_b32_e32 v39, v0
	v_mov_b32_e32 v40, v0
	v_mov_b32_e32 v41, v0
	v_mov_b32_e32 v42, v0
	v_mov_b32_e32 v43, v0
	v_mov_b32_e32 v44, v0
	v_mov_b32_e32 v45, v0
	v_mov_b32_e32 v46, v0
	v_mov_b32_e32 v47, v0
	v_mov_b32_e32 v48, v0
	v_mov_b32_e32 v49, v0
	v_mov_b32_e32 v50, v0
	v_mov_b32_e32 v51, v0
	v_mov_b32_e32 v52, v0
	v_mov_b32_e32 v53, v0
	v_mov_b32_e32 v54, v0
	v_mov_b32_e32 v55, v0
	v_mov_b32_e32 v56, v0
	v_mov_b32_e32 v57, v0
	v_mov_b32_e32 v58, v0
	v_mov_b32_e32 v59, v0
	v_mov_b32_e32 v60, v0
	v_mov_b32_e32 v61, v0
	v_mov_b32_e32 v62, v0
	v_mov_b32_e32 v63, v0
	v_mov_b32_e32 v160, v0
	v_mov_b32_e32 v161, v0
	v_mov_b32_e32 v227, v64
	v_mov_b32_e32 v228, v65
	v_mov_b32_e32 v229, v66
	v_mov_b32_e32 v184, v67
	v_readlane_b32 s100, v250, 8
	v_mbcnt_lo_u32_b32 v68, -1, 0
	v_mbcnt_hi_u32_b32 v68, -1, v68
	v_and_b32_e32 v69, 15, v68
	v_lshrrev_b32_e32 v70, 4, v68
	v_lshlrev_b32_e32 v72, 8, v69
	v_add_u32_e32 v72, 0x10000, v72
	v_add_u32_e32 v71, 0, v70
	v_xor_b32_e32 v71, v71, v69
	v_lshl_add_u32 v201, v71, 4, v72
	v_add_u32_e32 v71, 4, v70
	v_xor_b32_e32 v71, v71, v69
	v_lshl_add_u32 v202, v71, 4, v72
	v_add_u32_e32 v71, 8, v70
	v_xor_b32_e32 v71, v71, v69
	v_lshl_add_u32 v203, v71, 4, v72
	v_add_u32_e32 v71, 12, v70
	v_xor_b32_e32 v71, v71, v69
	v_lshl_add_u32 v246, v71, 4, v72
	v_bfe_u32 v73, v69, 1, 3
	v_lshlrev_b32_e32 v76, 7, v69
	v_add_u32_e32 v71, 0, v70
	v_xor_b32_e32 v71, v71, v73
	v_lshl_add_u32 v209, v71, 4, v76
	v_add_u32_e32 v71, 4, v70
	v_xor_b32_e32 v71, v71, v73
	v_lshl_add_u32 v210, v71, 4, v76
	s_lshl_b32 s101, s100, 7
	s_add_u32 s101, s101, 0x8000
	s_cmpk_ge_u32 s100, 0x100
	s_cselect_b32 s6, 0x8000, 0
	s_add_u32 s101, s101, s6
	v_and_b32_e32 v74, 31, v68
	v_lshrrev_b32_e32 v75, 5, v68
	v_lshlrev_b32_e32 v74, 8, v74
	v_lshl_add_u32 v74, v75, 4, v74
	v_add_u32_e32 v74, s101, v74
	v_lshlrev_b32_e32 v75, 8, v69
	v_lshl_add_u32 v75, v70, 4, v75
	v_add_u32_e32 v75, s101, v75
	ds_write_b128 v74, v[96:99] offset:0
	ds_write_b128 v74, v[100:103] offset:32
	ds_write_b128 v74, v[104:107] offset:64
	ds_write_b128 v74, v[108:111] offset:96
	ds_write_b128 v74, v[112:115] offset:128
	ds_write_b128 v74, v[116:119] offset:160
	ds_write_b128 v74, v[120:123] offset:192
	ds_write_b128 v74, v[124:127] offset:224
	s_waitcnt lgkmcnt(0)
	ds_read_b128 v[96:99], v75 offset:0
	ds_read_b128 v[100:103], v75 offset:64
	ds_read_b128 v[104:107], v75 offset:128
	ds_read_b128 v[108:111], v75 offset:192
	ds_read_b128 v[112:115], v75 offset:4096
	ds_read_b128 v[116:119], v75 offset:4160
	ds_read_b128 v[120:123], v75 offset:4224
	ds_read_b128 v[124:127], v75 offset:4288
	s_waitcnt vmcnt(0)
	s_waitcnt lgkmcnt(0)
	s_barrier
	ds_write_b128 v225, v[136:139] offset:32768
	ds_write_b128 v226, v[140:143] offset:32768
	s_add_u32 s15, s22, s12
	s_addc_u32 s14, s23, s13
	s_add_u32 s6, s15, 0x23a40000
	s_addc_u32 s7, s14, 0
	s_waitcnt lgkmcnt(0)
	global_load_dwordx4 v[136:139], v196, s[6:7]
	global_load_dwordx4 v[140:143], v197, s[6:7]
	v_mov_b32_e32 v194, 0
	v_mov_b32_e32 v195, 0
	s_barrier
	s_cmpk_ge_u32 s100, 0x100
	s_cselect_b32 s100, 1, 0
	ds_read_b128 v[160:163], v201 offset:0
	ds_read_b128 v[164:167], v202 offset:0
	ds_read_b128 v[168:171], v203 offset:0
	ds_read_b128 v[172:175], v246 offset:0
	ds_read_b128 v[176:179], v201 offset:4096
	ds_read_b128 v[180:183], v202 offset:4096
	ds_read_b128 v[230:233], v203 offset:4096
	s_waitcnt lgkmcnt(6)
	v_mfma_f32_16x16x32_bf16 v[64:67], v[160:163], v[96:99], 0
	v_mfma_f32_16x16x32_bf16 v[68:71], v[160:163], v[112:115], 0
	ds_read_b128 v[234:237], v246 offset:4096
	s_waitcnt lgkmcnt(6)
	v_mfma_f32_16x16x32_bf16 v[68:71], v[164:167], v[116:119], v[68:71]
	v_mfma_f32_16x16x32_bf16 v[64:67], v[164:167], v[100:103], v[64:67]
	ds_read_b128 v[160:163], v201 offset:8192
	s_waitcnt lgkmcnt(6)
	v_mfma_f32_16x16x32_bf16 v[64:67], v[168:171], v[104:107], v[64:67]
	v_mfma_f32_16x16x32_bf16 v[68:71], v[168:171], v[120:123], v[68:71]
	ds_read_b128 v[164:167], v202 offset:8192
	s_waitcnt lgkmcnt(6)
	v_mfma_f32_16x16x32_bf16 v[68:71], v[172:175], v[124:127], v[68:71]
	v_mfma_f32_16x16x32_bf16 v[64:67], v[172:175], v[108:111], v[64:67]
	ds_read_b128 v[168:171], v203 offset:8192
	s_waitcnt lgkmcnt(6)
	v_mfma_f32_16x16x32_bf16 v[72:75], v[176:179], v[96:99], 0
	s_nop 7
	s_nop 1
	v_exp_f32_e32 v64, v64
	v_mfma_f32_16x16x32_bf16 v[76:79], v[176:179], v[112:115], 0
	v_exp_f32_e32 v68, v68
	ds_read_b128 v[172:175], v246 offset:8192
	s_waitcnt lgkmcnt(6)
	v_mfma_f32_16x16x32_bf16 v[76:79], v[180:183], v[116:119], v[76:79]
	v_exp_f32_e32 v65, v65
	v_exp_f32_e32 v69, v69
	v_mfma_f32_16x16x32_bf16 v[72:75], v[180:183], v[100:103], v[72:75]
	v_exp_f32_e32 v66, v66
	ds_read_b128 v[176:179], v201 offset:12288
	s_waitcnt lgkmcnt(6)
	v_mfma_f32_16x16x32_bf16 v[72:75], v[230:233], v[104:107], v[72:75]
	v_exp_f32_e32 v70, v70
	v_exp_f32_e32 v67, v67
	v_mfma_f32_16x16x32_bf16 v[76:79], v[230:233], v[120:123], v[76:79]
	v_exp_f32_e32 v71, v71
	v_add_f32_e32 v220, v64, v65
	ds_read_b128 v[180:183], v202 offset:12288
	s_waitcnt lgkmcnt(6)
	v_mfma_f32_16x16x32_bf16 v[76:79], v[234:237], v[124:127], v[76:79]
	v_add_f32_e32 v221, v68, v69
	v_add_f32_e32 v220, v220, v66
	v_add_f32_e32 v221, v221, v70
	v_mfma_f32_16x16x32_bf16 v[72:75], v[234:237], v[108:111], v[72:75]
	v_add_f32_e32 v220, v220, v67
	v_add_f32_e32 v221, v221, v71
	ds_read_b128 v[230:233], v203 offset:12288
	s_waitcnt lgkmcnt(6)
	v_mfma_f32_16x16x32_bf16 v[80:83], v[160:163], v[96:99], 0
	s_nop 7
	s_nop 1
	v_exp_f32_e32 v72, v72
	v_exp_f32_e32 v76, v76
	v_mfma_f32_16x16x32_bf16 v[84:87], v[160:163], v[112:115], 0
	v_exp_f32_e32 v73, v73
	v_exp_f32_e32 v77, v77
	ds_read_b128 v[234:237], v246 offset:12288
	s_waitcnt lgkmcnt(6)
	v_mfma_f32_16x16x32_bf16 v[84:87], v[164:167], v[116:119], v[84:87]
	v_exp_f32_e32 v74, v74
	v_exp_f32_e32 v78, v78
	v_mfma_f32_16x16x32_bf16 v[80:83], v[164:167], v[100:103], v[80:83]
	v_exp_f32_e32 v75, v75
	v_exp_f32_e32 v79, v79
	s_waitcnt lgkmcnt(5)
	v_mfma_f32_16x16x32_bf16 v[80:83], v[168:171], v[104:107], v[80:83]
	v_add_f32_e32 v220, v220, v72
	v_add_f32_e32 v221, v221, v76
	v_add_f32_e32 v220, v220, v73
	v_add_f32_e32 v221, v221, v77
	v_mfma_f32_16x16x32_bf16 v[84:87], v[168:171], v[120:123], v[84:87]
	v_add_f32_e32 v220, v220, v74
	v_add_f32_e32 v221, v221, v78
	v_add_f32_e32 v220, v220, v75
	v_add_f32_e32 v221, v221, v79
	s_waitcnt lgkmcnt(4)
	v_mfma_f32_16x16x32_bf16 v[84:87], v[172:175], v[124:127], v[84:87]
	v_cvt_pk_bf16_f32 v216, v64, v65
	v_cvt_pk_bf16_f32 v217, v66, v67
	v_cvt_pk_bf16_f32 v238, v68, v69
	v_cvt_pk_bf16_f32 v239, v70, v71
	v_mfma_f32_16x16x32_bf16 v[80:83], v[172:175], v[108:111], v[80:83]
	v_cvt_pk_bf16_f32 v218, v72, v73
	v_cvt_pk_bf16_f32 v219, v74, v75
	v_cvt_pk_bf16_f32 v240, v76, v77
	v_cvt_pk_bf16_f32 v241, v78, v79
	s_waitcnt lgkmcnt(3)
	v_mfma_f32_16x16x32_bf16 v[88:91], v[176:179], v[96:99], 0
	s_nop 7
	s_nop 1
	v_exp_f32_e32 v80, v80
	v_exp_f32_e32 v84, v84
	v_mfma_f32_16x16x32_bf16 v[92:95], v[176:179], v[112:115], 0
	v_exp_f32_e32 v81, v81
	s_waitcnt lgkmcnt(2)
	v_mfma_f32_16x16x32_bf16 v[92:95], v[180:183], v[116:119], v[92:95]
	v_exp_f32_e32 v85, v85
	v_exp_f32_e32 v82, v82
	v_mfma_f32_16x16x32_bf16 v[88:91], v[180:183], v[100:103], v[88:91]
	v_exp_f32_e32 v86, v86
	s_waitcnt lgkmcnt(1)
	v_mfma_f32_16x16x32_bf16 v[88:91], v[230:233], v[104:107], v[88:91]
	v_exp_f32_e32 v83, v83
	v_exp_f32_e32 v87, v87
	v_mfma_f32_16x16x32_bf16 v[92:95], v[230:233], v[120:123], v[92:95]
	v_add_f32_e32 v220, v220, v80
	v_add_f32_e32 v221, v221, v84
	v_add_f32_e32 v220, v220, v81
	s_waitcnt lgkmcnt(0)
	v_mfma_f32_16x16x32_bf16 v[92:95], v[234:237], v[124:127], v[92:95]
	v_add_f32_e32 v221, v221, v85
	v_add_f32_e32 v220, v220, v82
	v_add_f32_e32 v221, v221, v86
	v_mfma_f32_16x16x32_bf16 v[88:91], v[234:237], v[108:111], v[88:91]
	v_add_f32_e32 v220, v220, v83
	v_add_f32_e32 v221, v221, v87
.LBB0_734:
	s_waitcnt lgkmcnt(0)
	s_barrier
	ds_read_b128 v[160:163], v201 offset:16384
	ds_read_b128 v[164:167], v209 offset:0
	ds_read_b128 v[168:171], v202 offset:16384
	ds_read_b128 v[172:175], v209 offset:2048
	ds_read_b128 v[176:179], v203 offset:16384
	ds_read_b128 v[180:183], v209 offset:4096
	ds_read_b128 v[230:233], v246 offset:16384
	s_cmp_eq_u32 s100, 0
	s_cbranch_scc1 .Lattn_pa0
	s_setprio 1
	s_branch .Lattn_pb0
.Lattn_pa0:
	s_setprio 0
.Lattn_pb0:
	s_waitcnt lgkmcnt(6)
	v_mfma_f32_16x16x32_bf16 v[64:67], v[160:163], v[96:99], 0
	v_exp_f32_e32 v88, v88
	v_mfma_f32_16x16x32_bf16 v[68:71], v[160:163], v[112:115], 0
	v_exp_f32_e32 v92, v92
	ds_read_b128 v[234:237], v209 offset:6144
	s_add_u32 s16, s22, s10
	s_addc_u32 s17, s23, s11
	s_add_u32 s15, s22, s12
	s_addc_u32 s14, s23, s13
	s_add_u32 s8, s16, 0x3bc00200
	s_addc_u32 s9, s17, 0
	s_add_u32 s6, s15, 0x23a50000
	s_addc_u32 s7, s14, 0
	s_waitcnt lgkmcnt(6)
	v_mfma_f32_16x16x32_bf16 v[0:3], v[164:167], v[216:219], v[0:3]
	v_cvt_pk_bf16_f32 v242, v80, v81
	v_mfma_f32_16x16x32_bf16 v[4:7], v[164:167], v[238:241], v[4:7]
	v_exp_f32_e32 v89, v89
	ds_read_b128 v[160:163], v201 offset:20480
	s_waitcnt vmcnt(4)
	ds_write_b128 v225, v[152:155] offset:49152
	s_waitcnt lgkmcnt(7)
	v_mfma_f32_16x16x32_bf16 v[68:71], v[168:171], v[116:119], v[68:71]
	v_exp_f32_e32 v93, v93
	v_mfma_f32_16x16x32_bf16 v[64:67], v[168:171], v[100:103], v[64:67]
	v_cvt_pk_bf16_f32 v243, v82, v83
	ds_read_b128 v[164:167], v209 offset:8192
	ds_write_b128 v226, v[156:159] offset:49152
	s_waitcnt lgkmcnt(8)
	v_mfma_f32_16x16x32_bf16 v[12:15], v[172:175], v[238:241], v[12:15]
	v_exp_f32_e32 v90, v90
	v_mfma_f32_16x16x32_bf16 v[8:11], v[172:175], v[216:219], v[8:11]
	v_exp_f32_e32 v94, v94
	ds_read_b128 v[168:171], v202 offset:20480
	ds_write_b64 v227, v[132:133] offset:32768
	s_waitcnt lgkmcnt(9)
	v_mfma_f32_16x16x32_bf16 v[64:67], v[176:179], v[104:107], v[64:67]
	v_cvt_pk_bf16_f32 v204, v84, v85
	v_mfma_f32_16x16x32_bf16 v[68:71], v[176:179], v[120:123], v[68:71]
	v_exp_f32_e32 v91, v91
	ds_read_b128 v[172:175], v209 offset:10240
	ds_write_b64 v228, v[134:135] offset:32768
	s_waitcnt lgkmcnt(10)
	v_mfma_f32_16x16x32_bf16 v[16:19], v[180:183], v[216:219], v[16:19]
	v_exp_f32_e32 v95, v95
	v_mfma_f32_16x16x32_bf16 v[20:23], v[180:183], v[238:241], v[20:23]
	v_cvt_pk_bf16_f32 v205, v86, v87
	v_add_f32_e32 v220, v220, v88
	ds_read_b128 v[176:179], v203 offset:20480
	ds_write_b64 v229, v[128:129] offset:32768
	s_waitcnt lgkmcnt(11)
	v_mfma_f32_16x16x32_bf16 v[68:71], v[230:233], v[124:127], v[68:71]
	v_add_f32_e32 v221, v221, v92
	v_add_f32_e32 v220, v220, v89
	v_mfma_f32_16x16x32_bf16 v[64:67], v[230:233], v[108:111], v[64:67]
	v_add_f32_e32 v221, v221, v93
	v_cvt_pk_bf16_f32 v244, v88, v89
	ds_read_b128 v[180:183], v209 offset:12288
	ds_write_b64 v184, v[130:131] offset:32768
	s_waitcnt lgkmcnt(12)
	v_mfma_f32_16x16x32_bf16 v[28:31], v[234:237], v[238:241], v[28:31]
	v_cvt_pk_bf16_f32 v245, v90, v91
	v_cvt_pk_bf16_f32 v206, v92, v93
	v_mfma_f32_16x16x32_bf16 v[24:27], v[234:237], v[216:219], v[24:27]
	v_cvt_pk_bf16_f32 v207, v94, v95
	ds_read_b128 v[230:233], v246 offset:20480
	global_load_dwordx4 v[132:135], v198, s[8:9]
	s_waitcnt lgkmcnt(12)
	v_mfma_f32_16x16x32_bf16 v[72:75], v[160:163], v[96:99], 0
	v_add_f32_e32 v220, v220, v90
	v_add_f32_e32 v221, v221, v94
	v_mfma_f32_16x16x32_bf16 v[76:79], v[160:163], v[112:115], 0
	v_add_f32_e32 v220, v220, v91
	v_add_f32_e32 v221, v221, v95
	ds_read_b128 v[234:237], v209 offset:14336
	global_load_dwordx4 v[128:131], v199, s[8:9]
	s_waitcnt lgkmcnt(11)
	v_mfma_f32_16x16x32_bf16 v[32:35], v[164:167], v[216:219], v[32:35]
	v_add_f32_e32 v194, v194, v220
	v_add_f32_e32 v195, v195, v221
	v_mfma_f32_16x16x32_bf16 v[36:39], v[164:167], v[238:241], v[36:39]
	v_exp_f32_e32 v64, v64
	ds_read_b128 v[160:163], v201 offset:24576
	global_load_dwordx4 v[152:155], v196, s[6:7]
	s_waitcnt lgkmcnt(10)
	v_mfma_f32_16x16x32_bf16 v[76:79], v[168:171], v[116:119], v[76:79]
	v_exp_f32_e32 v68, v68
	v_mfma_f32_16x16x32_bf16 v[72:75], v[168:171], v[100:103], v[72:75]
	v_exp_f32_e32 v65, v65
	ds_read_b128 v[164:167], v210 offset:0
	global_load_dwordx4 v[156:159], v197, s[6:7]
	s_waitcnt lgkmcnt(9)
	v_mfma_f32_16x16x32_bf16 v[44:47], v[172:175], v[238:241], v[44:47]
	v_exp_f32_e32 v69, v69
	v_mfma_f32_16x16x32_bf16 v[40:43], v[172:175], v[216:219], v[40:43]
	v_exp_f32_e32 v66, v66
	ds_read_b128 v[168:171], v202 offset:24576
	s_waitcnt lgkmcnt(8)
	v_mfma_f32_16x16x32_bf16 v[72:75], v[176:179], v[104:107], v[72:75]
	v_exp_f32_e32 v70, v70
	v_mfma_f32_16x16x32_bf16 v[76:79], v[176:179], v[120:123], v[76:79]
	v_exp_f32_e32 v67, v67
	ds_read_b128 v[172:175], v210 offset:2048
	s_waitcnt lgkmcnt(7)
	v_mfma_f32_16x16x32_bf16 v[48:51], v[180:183], v[216:219], v[48:51]
	v_exp_f32_e32 v71, v71
	v_mfma_f32_16x16x32_bf16 v[52:55], v[180:183], v[238:241], v[52:55]
	v_add_f32_e32 v220, v64, v65
	ds_read_b128 v[176:179], v203 offset:24576
	s_waitcnt lgkmcnt(6)
	v_mfma_f32_16x16x32_bf16 v[76:79], v[230:233], v[124:127], v[76:79]
	v_add_f32_e32 v221, v68, v69
	v_mfma_f32_16x16x32_bf16 v[72:75], v[230:233], v[108:111], v[72:75]
	v_add_f32_e32 v220, v220, v66
	ds_read_b128 v[180:183], v210 offset:4096
	s_waitcnt lgkmcnt(6)
	v_mfma_f32_16x16x32_bf16 v[60:63], v[234:237], v[238:241], v[60:63]
	v_add_f32_e32 v221, v221, v70
	v_add_f32_e32 v220, v220, v67
	v_mfma_f32_16x16x32_bf16 v[56:59], v[234:237], v[216:219], v[56:59]
	v_add_f32_e32 v221, v221, v71
	ds_read_b128 v[230:233], v246 offset:24576
	s_waitcnt lgkmcnt(6)
	v_mfma_f32_16x16x32_bf16 v[80:83], v[160:163], v[96:99], 0
	v_exp_f32_e32 v72, v72
	v_mfma_f32_16x16x32_bf16 v[84:87], v[160:163], v[112:115], 0
	v_exp_f32_e32 v76, v76
	ds_read_b128 v[234:237], v210 offset:6144
	s_waitcnt lgkmcnt(6)
	v_mfma_f32_16x16x32_bf16 v[0:3], v[164:167], v[242:245], v[0:3]
	v_exp_f32_e32 v73, v73
	v_mfma_f32_16x16x32_bf16 v[4:7], v[164:167], v[204:207], v[4:7]
	v_exp_f32_e32 v77, v77
	ds_read_b128 v[160:163], v201 offset:28672
	s_waitcnt lgkmcnt(6)
	v_mfma_f32_16x16x32_bf16 v[84:87], v[168:171], v[116:119], v[84:87]
	v_exp_f32_e32 v74, v74
	v_mfma_f32_16x16x32_bf16 v[80:83], v[168:171], v[100:103], v[80:83]
	v_exp_f32_e32 v78, v78
	ds_read_b128 v[164:167], v210 offset:8192
	s_waitcnt lgkmcnt(6)
	v_mfma_f32_16x16x32_bf16 v[12:15], v[172:175], v[204:207], v[12:15]
	v_exp_f32_e32 v75, v75
	v_mfma_f32_16x16x32_bf16 v[8:11], v[172:175], v[242:245], v[8:11]
	v_exp_f32_e32 v79, v79
	ds_read_b128 v[168:171], v202 offset:28672
	s_waitcnt lgkmcnt(6)
	v_mfma_f32_16x16x32_bf16 v[80:83], v[176:179], v[104:107], v[80:83]
	v_add_f32_e32 v220, v220, v72
	v_add_f32_e32 v221, v221, v76
	v_mfma_f32_16x16x32_bf16 v[84:87], v[176:179], v[120:123], v[84:87]
	v_add_f32_e32 v220, v220, v73
	ds_read_b128 v[172:175], v210 offset:10240
	s_waitcnt lgkmcnt(6)
	v_mfma_f32_16x16x32_bf16 v[16:19], v[180:183], v[242:245], v[16:19]
	v_add_f32_e32 v221, v221, v77
	v_add_f32_e32 v220, v220, v74
	v_mfma_f32_16x16x32_bf16 v[20:23], v[180:183], v[204:207], v[20:23]
	v_add_f32_e32 v221, v221, v78
	ds_read_b128 v[176:179], v203 offset:28672
	s_waitcnt lgkmcnt(6)
	v_mfma_f32_16x16x32_bf16 v[84:87], v[230:233], v[124:127], v[84:87]
	v_add_f32_e32 v220, v220, v75
	v_add_f32_e32 v221, v221, v79
	v_mfma_f32_16x16x32_bf16 v[80:83], v[230:233], v[108:111], v[80:83]
	v_cvt_pk_bf16_f32 v216, v64, v65
	ds_read_b128 v[180:183], v210 offset:12288
	s_waitcnt lgkmcnt(6)
	v_mfma_f32_16x16x32_bf16 v[28:31], v[234:237], v[204:207], v[28:31]
	v_cvt_pk_bf16_f32 v217, v66, v67
	v_cvt_pk_bf16_f32 v238, v68, v69
	v_mfma_f32_16x16x32_bf16 v[24:27], v[234:237], v[242:245], v[24:27]
	v_cvt_pk_bf16_f32 v239, v70, v71
	ds_read_b128 v[230:233], v246 offset:28672
	s_waitcnt lgkmcnt(6)
	v_mfma_f32_16x16x32_bf16 v[88:91], v[160:163], v[96:99], 0
	v_exp_f32_e32 v80, v80
	v_mfma_f32_16x16x32_bf16 v[92:95], v[160:163], v[112:115], 0
	v_exp_f32_e32 v84, v84
	ds_read_b128 v[234:237], v210 offset:14336
	s_waitcnt lgkmcnt(6)
	v_mfma_f32_16x16x32_bf16 v[32:35], v[164:167], v[242:245], v[32:35]
	v_exp_f32_e32 v81, v81
	v_mfma_f32_16x16x32_bf16 v[36:39], v[164:167], v[204:207], v[36:39]
	v_exp_f32_e32 v85, v85
	ds_read_b128 v[160:163], v201 offset:32768
	s_waitcnt lgkmcnt(6)
	v_mfma_f32_16x16x32_bf16 v[92:95], v[168:171], v[116:119], v[92:95]
	v_exp_f32_e32 v82, v82
	v_mfma_f32_16x16x32_bf16 v[88:91], v[168:171], v[100:103], v[88:91]
	v_exp_f32_e32 v86, v86
	ds_read_b128 v[164:167], v209 offset:16384
	s_waitcnt lgkmcnt(6)
	v_mfma_f32_16x16x32_bf16 v[44:47], v[172:175], v[204:207], v[44:47]
	v_exp_f32_e32 v83, v83
	v_mfma_f32_16x16x32_bf16 v[40:43], v[172:175], v[242:245], v[40:43]
	v_exp_f32_e32 v87, v87
	ds_read_b128 v[168:171], v202 offset:32768
	s_waitcnt lgkmcnt(6)
	v_mfma_f32_16x16x32_bf16 v[88:91], v[176:179], v[104:107], v[88:91]
	v_add_f32_e32 v220, v220, v80
	v_add_f32_e32 v221, v221, v84
	v_mfma_f32_16x16x32_bf16 v[92:95], v[176:179], v[120:123], v[92:95]
	v_add_f32_e32 v220, v220, v81
	ds_read_b128 v[172:175], v209 offset:18432
	s_waitcnt lgkmcnt(6)
	v_mfma_f32_16x16x32_bf16 v[48:51], v[180:183], v[242:245], v[48:51]
	v_add_f32_e32 v221, v221, v85
	v_add_f32_e32 v220, v220, v82
	v_mfma_f32_16x16x32_bf16 v[52:55], v[180:183], v[204:207], v[52:55]
	v_add_f32_e32 v221, v221, v86
	ds_read_b128 v[176:179], v203 offset:32768
	s_waitcnt lgkmcnt(6)
	v_mfma_f32_16x16x32_bf16 v[92:95], v[230:233], v[124:127], v[92:95]
	v_add_f32_e32 v220, v220, v83
	v_add_f32_e32 v221, v221, v87
	v_mfma_f32_16x16x32_bf16 v[88:91], v[230:233], v[108:111], v[88:91]
	v_cvt_pk_bf16_f32 v218, v72, v73
	ds_read_b128 v[180:183], v209 offset:20480
	s_waitcnt lgkmcnt(6)
	v_mfma_f32_16x16x32_bf16 v[60:63], v[234:237], v[204:207], v[60:63]
	v_cvt_pk_bf16_f32 v219, v74, v75
	v_cvt_pk_bf16_f32 v240, v76, v77
	v_mfma_f32_16x16x32_bf16 v[56:59], v[234:237], v[242:245], v[56:59]
	v_cvt_pk_bf16_f32 v241, v78, v79
	ds_read_b128 v[230:233], v246 offset:32768
	s_cmp_eq_u32 s100, 1
	s_cbranch_scc1 .Lattn_pa1
	s_setprio 1
	s_branch .Lattn_pb1

.Lattn_pb1:
	s_waitcnt lgkmcnt(6)
	v_mfma_f32_16x16x32_bf16 v[64:67], v[160:163], v[96:99], 0
	v_exp_f32_e32 v88, v88
	v_mfma_f32_16x16x32_bf16 v[68:71], v[160:163], v[112:115], 0
	v_exp_f32_e32 v92, v92
	ds_read_b128 v[234:237], v209 offset:22528
	s_add_u32 s8, s16, 0x3bc00280
	s_addc_u32 s9, s17, 0
	s_add_u32 s6, s15, 0x23a60000
	s_addc_u32 s7, s14, 0
	s_waitcnt lgkmcnt(6)
	v_mfma_f32_16x16x32_bf16 v[0:3], v[164:167], v[216:219], v[0:3]
	v_cvt_pk_bf16_f32 v242, v80, v81
	v_mfma_f32_16x16x32_bf16 v[4:7], v[164:167], v[238:241], v[4:7]
	v_exp_f32_e32 v89, v89
	ds_read_b128 v[160:163], v201 offset:36864
	s_waitcnt vmcnt(4)
	ds_write_b128 v225, v[136:139] offset:0
	s_waitcnt lgkmcnt(7)
	v_mfma_f32_16x16x32_bf16 v[68:71], v[168:171], v[116:119], v[68:71]
	v_exp_f32_e32 v93, v93
	v_mfma_f32_16x16x32_bf16 v[64:67], v[168:171], v[100:103], v[64:67]
	v_cvt_pk_bf16_f32 v243, v82, v83
	ds_read_b128 v[164:167], v209 offset:24576
	ds_write_b128 v226, v[140:143] offset:0
	s_waitcnt lgkmcnt(8)
	v_mfma_f32_16x16x32_bf16 v[12:15], v[172:175], v[238:241], v[12:15]
	v_exp_f32_e32 v90, v90
	v_mfma_f32_16x16x32_bf16 v[8:11], v[172:175], v[216:219], v[8:11]
	v_exp_f32_e32 v94, v94
	ds_read_b128 v[168:171], v202 offset:36864
	ds_write_b64 v227, v[148:149] offset:49152
	s_waitcnt lgkmcnt(9)
	v_mfma_f32_16x16x32_bf16 v[64:67], v[176:179], v[104:107], v[64:67]
	v_cvt_pk_bf16_f32 v204, v84, v85
	v_mfma_f32_16x16x32_bf16 v[68:71], v[176:179], v[120:123], v[68:71]
	v_exp_f32_e32 v91, v91
	ds_read_b128 v[172:175], v209 offset:26624
	ds_write_b64 v228, v[150:151] offset:49152
	s_waitcnt lgkmcnt(10)
	v_mfma_f32_16x16x32_bf16 v[16:19], v[180:183], v[216:219], v[16:19]
	v_exp_f32_e32 v95, v95
	v_mfma_f32_16x16x32_bf16 v[20:23], v[180:183], v[238:241], v[20:23]
	v_cvt_pk_bf16_f32 v205, v86, v87
	v_add_f32_e32 v220, v220, v88
	ds_read_b128 v[176:179], v203 offset:36864
	ds_write_b64 v229, v[144:145] offset:49152
	s_waitcnt lgkmcnt(11)
	v_mfma_f32_16x16x32_bf16 v[68:71], v[230:233], v[124:127], v[68:71]
	v_add_f32_e32 v221, v221, v92
	v_add_f32_e32 v220, v220, v89
	v_mfma_f32_16x16x32_bf16 v[64:67], v[230:233], v[108:111], v[64:67]
	v_add_f32_e32 v221, v221, v93
	v_cvt_pk_bf16_f32 v244, v88, v89
	ds_read_b128 v[180:183], v209 offset:28672
	ds_write_b64 v184, v[146:147] offset:49152
	s_waitcnt lgkmcnt(12)
	v_mfma_f32_16x16x32_bf16 v[28:31], v[234:237], v[238:241], v[28:31]
	v_cvt_pk_bf16_f32 v245, v90, v91
	v_cvt_pk_bf16_f32 v206, v92, v93
	v_mfma_f32_16x16x32_bf16 v[24:27], v[234:237], v[216:219], v[24:27]
	v_cvt_pk_bf16_f32 v207, v94, v95
	ds_read_b128 v[230:233], v246 offset:36864
	global_load_dwordx4 v[148:151], v198, s[8:9]
	s_waitcnt lgkmcnt(12)
	v_mfma_f32_16x16x32_bf16 v[72:75], v[160:163], v[96:99], 0
	v_add_f32_e32 v220, v220, v90
	v_add_f32_e32 v221, v221, v94
	v_mfma_f32_16x16x32_bf16 v[76:79], v[160:163], v[112:115], 0
	v_add_f32_e32 v220, v220, v91
	v_add_f32_e32 v221, v221, v95
	ds_read_b128 v[234:237], v209 offset:30720
	global_load_dwordx4 v[144:147], v199, s[8:9]
	s_waitcnt lgkmcnt(11)
	v_mfma_f32_16x16x32_bf16 v[32:35], v[164:167], v[216:219], v[32:35]
	v_add_f32_e32 v194, v194, v220
	v_add_f32_e32 v195, v195, v221
	v_mfma_f32_16x16x32_bf16 v[36:39], v[164:167], v[238:241], v[36:39]
	v_exp_f32_e32 v64, v64
	ds_read_b128 v[160:163], v201 offset:40960
	global_load_dwordx4 v[136:139], v196, s[6:7]
	s_waitcnt lgkmcnt(10)
	v_mfma_f32_16x16x32_bf16 v[76:79], v[168:171], v[116:119], v[76:79]
	v_exp_f32_e32 v68, v68
	v_mfma_f32_16x16x32_bf16 v[72:75], v[168:171], v[100:103], v[72:75]
	v_exp_f32_e32 v65, v65
	ds_read_b128 v[164:167], v210 offset:16384
	global_load_dwordx4 v[140:143], v197, s[6:7]
	s_waitcnt lgkmcnt(9)
	v_mfma_f32_16x16x32_bf16 v[44:47], v[172:175], v[238:241], v[44:47]
	v_exp_f32_e32 v69, v69
	v_mfma_f32_16x16x32_bf16 v[40:43], v[172:175], v[216:219], v[40:43]
	v_exp_f32_e32 v66, v66
	ds_read_b128 v[168:171], v202 offset:40960
	s_waitcnt lgkmcnt(8)
	v_mfma_f32_16x16x32_bf16 v[72:75], v[176:179], v[104:107], v[72:75]
	v_exp_f32_e32 v70, v70
	v_mfma_f32_16x16x32_bf16 v[76:79], v[176:179], v[120:123], v[76:79]
	v_exp_f32_e32 v67, v67
	ds_read_b128 v[172:175], v210 offset:18432
	s_waitcnt lgkmcnt(7)
	v_mfma_f32_16x16x32_bf16 v[48:51], v[180:183], v[216:219], v[48:51]
	v_exp_f32_e32 v71, v71
	v_mfma_f32_16x16x32_bf16 v[52:55], v[180:183], v[238:241], v[52:55]
	v_add_f32_e32 v220, v64, v65
	ds_read_b128 v[176:179], v203 offset:40960
	s_waitcnt lgkmcnt(6)
	v_mfma_f32_16x16x32_bf16 v[76:79], v[230:233], v[124:127], v[76:79]
	v_add_f32_e32 v221, v68, v69
	v_mfma_f32_16x16x32_bf16 v[72:75], v[230:233], v[108:111], v[72:75]
	v_add_f32_e32 v220, v220, v66
	ds_read_b128 v[180:183], v210 offset:20480
	s_waitcnt lgkmcnt(6)
	v_mfma_f32_16x16x32_bf16 v[60:63], v[234:237], v[238:241], v[60:63]
	v_add_f32_e32 v221, v221, v70
	v_add_f32_e32 v220, v220, v67
	v_mfma_f32_16x16x32_bf16 v[56:59], v[234:237], v[216:219], v[56:59]
	v_add_f32_e32 v221, v221, v71
	ds_read_b128 v[230:233], v246 offset:40960
	s_waitcnt lgkmcnt(6)
	v_mfma_f32_16x16x32_bf16 v[80:83], v[160:163], v[96:99], 0
	v_exp_f32_e32 v72, v72
	v_mfma_f32_16x16x32_bf16 v[84:87], v[160:163], v[112:115], 0
	v_exp_f32_e32 v76, v76
	ds_read_b128 v[234:237], v210 offset:22528
	s_waitcnt lgkmcnt(6)
	v_mfma_f32_16x16x32_bf16 v[0:3], v[164:167], v[242:245], v[0:3]
	v_exp_f32_e32 v73, v73
	v_mfma_f32_16x16x32_bf16 v[4:7], v[164:167], v[204:207], v[4:7]
	v_exp_f32_e32 v77, v77
	ds_read_b128 v[160:163], v201 offset:45056
	s_waitcnt lgkmcnt(6)
	v_mfma_f32_16x16x32_bf16 v[84:87], v[168:171], v[116:119], v[84:87]
	v_exp_f32_e32 v74, v74
	v_mfma_f32_16x16x32_bf16 v[80:83], v[168:171], v[100:103], v[80:83]
	v_exp_f32_e32 v78, v78
	ds_read_b128 v[164:167], v210 offset:24576
	s_waitcnt lgkmcnt(6)
	v_mfma_f32_16x16x32_bf16 v[12:15], v[172:175], v[204:207], v[12:15]
	v_exp_f32_e32 v75, v75
	v_mfma_f32_16x16x32_bf16 v[8:11], v[172:175], v[242:245], v[8:11]
	v_exp_f32_e32 v79, v79
	ds_read_b128 v[168:171], v202 offset:45056
	s_waitcnt lgkmcnt(6)
	v_mfma_f32_16x16x32_bf16 v[80:83], v[176:179], v[104:107], v[80:83]
	v_add_f32_e32 v220, v220, v72
	v_add_f32_e32 v221, v221, v76
	v_mfma_f32_16x16x32_bf16 v[84:87], v[176:179], v[120:123], v[84:87]
	v_add_f32_e32 v220, v220, v73
	ds_read_b128 v[172:175], v210 offset:26624
	s_waitcnt lgkmcnt(6)
	v_mfma_f32_16x16x32_bf16 v[16:19], v[180:183], v[242:245], v[16:19]
	v_add_f32_e32 v221, v221, v77
	v_add_f32_e32 v220, v220, v74
	v_mfma_f32_16x16x32_bf16 v[20:23], v[180:183], v[204:207], v[20:23]
	v_add_f32_e32 v221, v221, v78
	ds_read_b128 v[176:179], v203 offset:45056
	s_waitcnt lgkmcnt(6)
	v_mfma_f32_16x16x32_bf16 v[84:87], v[230:233], v[124:127], v[84:87]
	v_add_f32_e32 v220, v220, v75
	v_add_f32_e32 v221, v221, v79
	v_mfma_f32_16x16x32_bf16 v[80:83], v[230:233], v[108:111], v[80:83]
	v_cvt_pk_bf16_f32 v216, v64, v65
	ds_read_b128 v[180:183], v210 offset:28672
	s_waitcnt lgkmcnt(6)
	v_mfma_f32_16x16x32_bf16 v[28:31], v[234:237], v[204:207], v[28:31]
	v_cvt_pk_bf16_f32 v217, v66, v67
	v_cvt_pk_bf16_f32 v238, v68, v69
	v_mfma_f32_16x16x32_bf16 v[24:27], v[234:237], v[242:245], v[24:27]
	v_cvt_pk_bf16_f32 v239, v70, v71
	ds_read_b128 v[230:233], v246 offset:45056
	s_waitcnt lgkmcnt(6)
	v_mfma_f32_16x16x32_bf16 v[88:91], v[160:163], v[96:99], 0
	v_exp_f32_e32 v80, v80
	v_mfma_f32_16x16x32_bf16 v[92:95], v[160:163], v[112:115], 0
	v_exp_f32_e32 v84, v84
	ds_read_b128 v[234:237], v210 offset:30720
	s_waitcnt lgkmcnt(6)
	v_mfma_f32_16x16x32_bf16 v[32:35], v[164:167], v[242:245], v[32:35]
	v_exp_f32_e32 v81, v81
	v_mfma_f32_16x16x32_bf16 v[36:39], v[164:167], v[204:207], v[36:39]
	v_exp_f32_e32 v85, v85
	s_waitcnt lgkmcnt(5)
	v_mfma_f32_16x16x32_bf16 v[92:95], v[168:171], v[116:119], v[92:95]
	v_exp_f32_e32 v82, v82
	v_mfma_f32_16x16x32_bf16 v[88:91], v[168:171], v[100:103], v[88:91]
	v_exp_f32_e32 v86, v86
	s_waitcnt lgkmcnt(4)
	v_mfma_f32_16x16x32_bf16 v[44:47], v[172:175], v[204:207], v[44:47]
	v_exp_f32_e32 v83, v83
	v_mfma_f32_16x16x32_bf16 v[40:43], v[172:175], v[242:245], v[40:43]
	v_exp_f32_e32 v87, v87
	s_waitcnt lgkmcnt(3)
	v_mfma_f32_16x16x32_bf16 v[88:91], v[176:179], v[104:107], v[88:91]
	v_add_f32_e32 v220, v220, v80
	v_add_f32_e32 v221, v221, v84
	v_mfma_f32_16x16x32_bf16 v[92:95], v[176:179], v[120:123], v[92:95]
	v_add_f32_e32 v220, v220, v81
	s_waitcnt lgkmcnt(2)
	v_mfma_f32_16x16x32_bf16 v[48:51], v[180:183], v[242:245], v[48:51]
	v_add_f32_e32 v221, v221, v85
	v_add_f32_e32 v220, v220, v82
	v_mfma_f32_16x16x32_bf16 v[52:55], v[180:183], v[204:207], v[52:55]
	v_add_f32_e32 v221, v221, v86
	s_waitcnt lgkmcnt(1)
	v_mfma_f32_16x16x32_bf16 v[92:95], v[230:233], v[124:127], v[92:95]
	v_add_f32_e32 v220, v220, v83
	v_add_f32_e32 v221, v221, v87
	v_mfma_f32_16x16x32_bf16 v[88:91], v[230:233], v[108:111], v[88:91]
	v_cvt_pk_bf16_f32 v218, v72, v73
	s_waitcnt lgkmcnt(0)
	v_mfma_f32_16x16x32_bf16 v[60:63], v[234:237], v[204:207], v[60:63]
	v_cvt_pk_bf16_f32 v219, v74, v75
	v_cvt_pk_bf16_f32 v240, v76, v77
	v_mfma_f32_16x16x32_bf16 v[56:59], v[234:237], v[242:245], v[56:59]
	v_cvt_pk_bf16_f32 v241, v78, v79
	s_waitcnt lgkmcnt(0)
	s_barrier
	ds_read_b128 v[160:163], v201 offset:49152
	ds_read_b128 v[164:167], v209 offset:32768
	ds_read_b128 v[168:171], v202 offset:49152
	ds_read_b128 v[172:175], v209 offset:34816
	ds_read_b128 v[176:179], v203 offset:49152
	ds_read_b128 v[180:183], v209 offset:36864
	ds_read_b128 v[230:233], v246 offset:49152
	s_cmp_eq_u32 s100, 0
	s_cbranch_scc1 .Lattn_pa2
	s_setprio 1
	s_branch .Lattn_pb2

.Lattn_pb2:
	s_waitcnt lgkmcnt(6)
	v_mfma_f32_16x16x32_bf16 v[64:67], v[160:163], v[96:99], 0
	v_exp_f32_e32 v88, v88
	v_mfma_f32_16x16x32_bf16 v[68:71], v[160:163], v[112:115], 0
	v_exp_f32_e32 v92, v92
	ds_read_b128 v[234:237], v209 offset:38912
	s_add_u32 s8, s16, 0x3bc00300
	s_addc_u32 s9, s17, 0
	s_add_u32 s6, s15, 0x23a70000
	s_addc_u32 s7, s14, 0
	s_waitcnt lgkmcnt(6)
	v_mfma_f32_16x16x32_bf16 v[0:3], v[164:167], v[216:219], v[0:3]
	v_cvt_pk_bf16_f32 v242, v80, v81
	v_mfma_f32_16x16x32_bf16 v[4:7], v[164:167], v[238:241], v[4:7]
	v_exp_f32_e32 v89, v89
	ds_read_b128 v[160:163], v201 offset:53248
	s_waitcnt vmcnt(4)
	ds_write_b128 v225, v[152:155] offset:16384
	s_waitcnt lgkmcnt(7)
	v_mfma_f32_16x16x32_bf16 v[68:71], v[168:171], v[116:119], v[68:71]
	v_exp_f32_e32 v93, v93
	v_mfma_f32_16x16x32_bf16 v[64:67], v[168:171], v[100:103], v[64:67]
	v_cvt_pk_bf16_f32 v243, v82, v83
	ds_read_b128 v[164:167], v209 offset:40960
	ds_write_b128 v226, v[156:159] offset:16384
	s_waitcnt lgkmcnt(8)
	v_mfma_f32_16x16x32_bf16 v[12:15], v[172:175], v[238:241], v[12:15]
	v_exp_f32_e32 v90, v90
	v_mfma_f32_16x16x32_bf16 v[8:11], v[172:175], v[216:219], v[8:11]
	v_exp_f32_e32 v94, v94
	ds_read_b128 v[168:171], v202 offset:53248
	ds_write_b64 v227, v[132:133] offset:0
	s_waitcnt lgkmcnt(9)
	v_mfma_f32_16x16x32_bf16 v[64:67], v[176:179], v[104:107], v[64:67]
	v_cvt_pk_bf16_f32 v204, v84, v85
	v_mfma_f32_16x16x32_bf16 v[68:71], v[176:179], v[120:123], v[68:71]
	v_exp_f32_e32 v91, v91
	ds_read_b128 v[172:175], v209 offset:43008
	ds_write_b64 v228, v[134:135] offset:0
	s_waitcnt lgkmcnt(10)
	v_mfma_f32_16x16x32_bf16 v[16:19], v[180:183], v[216:219], v[16:19]
	v_exp_f32_e32 v95, v95
	v_mfma_f32_16x16x32_bf16 v[20:23], v[180:183], v[238:241], v[20:23]
	v_cvt_pk_bf16_f32 v205, v86, v87
	v_add_f32_e32 v220, v220, v88
	ds_read_b128 v[176:179], v203 offset:53248
	ds_write_b64 v229, v[128:129] offset:0
	s_waitcnt lgkmcnt(11)
	v_mfma_f32_16x16x32_bf16 v[68:71], v[230:233], v[124:127], v[68:71]
	v_add_f32_e32 v221, v221, v92
	v_add_f32_e32 v220, v220, v89
	v_mfma_f32_16x16x32_bf16 v[64:67], v[230:233], v[108:111], v[64:67]
	v_add_f32_e32 v221, v221, v93
	v_cvt_pk_bf16_f32 v244, v88, v89
	ds_read_b128 v[180:183], v209 offset:45056
	ds_write_b64 v184, v[130:131] offset:0
	s_waitcnt lgkmcnt(12)
	v_mfma_f32_16x16x32_bf16 v[28:31], v[234:237], v[238:241], v[28:31]
	v_cvt_pk_bf16_f32 v245, v90, v91
	v_cvt_pk_bf16_f32 v206, v92, v93
	v_mfma_f32_16x16x32_bf16 v[24:27], v[234:237], v[216:219], v[24:27]
	v_cvt_pk_bf16_f32 v207, v94, v95
	ds_read_b128 v[230:233], v246 offset:53248
	global_load_dwordx4 v[132:135], v198, s[8:9]
	s_waitcnt lgkmcnt(12)
	v_mfma_f32_16x16x32_bf16 v[72:75], v[160:163], v[96:99], 0
	v_add_f32_e32 v220, v220, v90
	v_add_f32_e32 v221, v221, v94
	v_mfma_f32_16x16x32_bf16 v[76:79], v[160:163], v[112:115], 0
	v_add_f32_e32 v220, v220, v91
	v_add_f32_e32 v221, v221, v95
	ds_read_b128 v[234:237], v209 offset:47104
	global_load_dwordx4 v[128:131], v199, s[8:9]
	s_waitcnt lgkmcnt(11)
	v_mfma_f32_16x16x32_bf16 v[32:35], v[164:167], v[216:219], v[32:35]
	v_add_f32_e32 v194, v194, v220
	v_add_f32_e32 v195, v195, v221
	v_mfma_f32_16x16x32_bf16 v[36:39], v[164:167], v[238:241], v[36:39]
	v_exp_f32_e32 v64, v64
	ds_read_b128 v[160:163], v201 offset:57344
	global_load_dwordx4 v[152:155], v196, s[6:7]
	s_waitcnt lgkmcnt(10)
	v_mfma_f32_16x16x32_bf16 v[76:79], v[168:171], v[116:119], v[76:79]
	v_exp_f32_e32 v68, v68
	v_mfma_f32_16x16x32_bf16 v[72:75], v[168:171], v[100:103], v[72:75]
	v_exp_f32_e32 v65, v65
	ds_read_b128 v[164:167], v210 offset:32768
	global_load_dwordx4 v[156:159], v197, s[6:7]
	s_waitcnt lgkmcnt(9)
	v_mfma_f32_16x16x32_bf16 v[44:47], v[172:175], v[238:241], v[44:47]
	v_exp_f32_e32 v69, v69
	v_mfma_f32_16x16x32_bf16 v[40:43], v[172:175], v[216:219], v[40:43]
	v_exp_f32_e32 v66, v66
	ds_read_b128 v[168:171], v202 offset:57344
	s_waitcnt lgkmcnt(8)
	v_mfma_f32_16x16x32_bf16 v[72:75], v[176:179], v[104:107], v[72:75]
	v_exp_f32_e32 v70, v70
	v_mfma_f32_16x16x32_bf16 v[76:79], v[176:179], v[120:123], v[76:79]
	v_exp_f32_e32 v67, v67
	ds_read_b128 v[172:175], v210 offset:34816
	s_waitcnt lgkmcnt(7)
	v_mfma_f32_16x16x32_bf16 v[48:51], v[180:183], v[216:219], v[48:51]
	v_exp_f32_e32 v71, v71
	v_mfma_f32_16x16x32_bf16 v[52:55], v[180:183], v[238:241], v[52:55]
	v_add_f32_e32 v220, v64, v65
	ds_read_b128 v[176:179], v203 offset:57344
	s_waitcnt lgkmcnt(6)
	v_mfma_f32_16x16x32_bf16 v[76:79], v[230:233], v[124:127], v[76:79]
	v_add_f32_e32 v221, v68, v69
	v_mfma_f32_16x16x32_bf16 v[72:75], v[230:233], v[108:111], v[72:75]
	v_add_f32_e32 v220, v220, v66
	ds_read_b128 v[180:183], v210 offset:36864
	s_waitcnt lgkmcnt(6)
	v_mfma_f32_16x16x32_bf16 v[60:63], v[234:237], v[238:241], v[60:63]
	v_add_f32_e32 v221, v221, v70
	v_add_f32_e32 v220, v220, v67
	v_mfma_f32_16x16x32_bf16 v[56:59], v[234:237], v[216:219], v[56:59]
	v_add_f32_e32 v221, v221, v71
	ds_read_b128 v[230:233], v246 offset:57344
	s_waitcnt lgkmcnt(6)
	v_mfma_f32_16x16x32_bf16 v[80:83], v[160:163], v[96:99], 0
	v_exp_f32_e32 v72, v72
	v_mfma_f32_16x16x32_bf16 v[84:87], v[160:163], v[112:115], 0
	v_exp_f32_e32 v76, v76
	ds_read_b128 v[234:237], v210 offset:38912
	s_waitcnt lgkmcnt(6)
	v_mfma_f32_16x16x32_bf16 v[0:3], v[164:167], v[242:245], v[0:3]
	v_exp_f32_e32 v73, v73
	v_mfma_f32_16x16x32_bf16 v[4:7], v[164:167], v[204:207], v[4:7]
	v_exp_f32_e32 v77, v77
	ds_read_b128 v[160:163], v201 offset:61440
	s_waitcnt lgkmcnt(6)
	v_mfma_f32_16x16x32_bf16 v[84:87], v[168:171], v[116:119], v[84:87]
	v_exp_f32_e32 v74, v74
	v_mfma_f32_16x16x32_bf16 v[80:83], v[168:171], v[100:103], v[80:83]
	v_exp_f32_e32 v78, v78
	ds_read_b128 v[164:167], v210 offset:40960
	s_waitcnt lgkmcnt(6)
	v_mfma_f32_16x16x32_bf16 v[12:15], v[172:175], v[204:207], v[12:15]
	v_exp_f32_e32 v75, v75
	v_mfma_f32_16x16x32_bf16 v[8:11], v[172:175], v[242:245], v[8:11]
	v_exp_f32_e32 v79, v79
	ds_read_b128 v[168:171], v202 offset:61440
	s_waitcnt lgkmcnt(6)
	v_mfma_f32_16x16x32_bf16 v[80:83], v[176:179], v[104:107], v[80:83]
	v_add_f32_e32 v220, v220, v72
	v_add_f32_e32 v221, v221, v76
	v_mfma_f32_16x16x32_bf16 v[84:87], v[176:179], v[120:123], v[84:87]
	v_add_f32_e32 v220, v220, v73
	ds_read_b128 v[172:175], v210 offset:43008
	s_waitcnt lgkmcnt(6)
	v_mfma_f32_16x16x32_bf16 v[16:19], v[180:183], v[242:245], v[16:19]
	v_add_f32_e32 v221, v221, v77
	v_add_f32_e32 v220, v220, v74
	v_mfma_f32_16x16x32_bf16 v[20:23], v[180:183], v[204:207], v[20:23]
	v_add_f32_e32 v221, v221, v78
	ds_read_b128 v[176:179], v203 offset:61440
	s_waitcnt lgkmcnt(6)
	v_mfma_f32_16x16x32_bf16 v[84:87], v[230:233], v[124:127], v[84:87]
	v_add_f32_e32 v220, v220, v75
	v_add_f32_e32 v221, v221, v79
	v_mfma_f32_16x16x32_bf16 v[80:83], v[230:233], v[108:111], v[80:83]
	v_cvt_pk_bf16_f32 v216, v64, v65
	ds_read_b128 v[180:183], v210 offset:45056
	s_waitcnt lgkmcnt(6)
	v_mfma_f32_16x16x32_bf16 v[28:31], v[234:237], v[204:207], v[28:31]
	v_cvt_pk_bf16_f32 v217, v66, v67
	v_cvt_pk_bf16_f32 v238, v68, v69
	v_mfma_f32_16x16x32_bf16 v[24:27], v[234:237], v[242:245], v[24:27]
	v_cvt_pk_bf16_f32 v239, v70, v71
	ds_read_b128 v[230:233], v246 offset:61440
	s_waitcnt lgkmcnt(6)
	v_mfma_f32_16x16x32_bf16 v[88:91], v[160:163], v[96:99], 0
	v_exp_f32_e32 v80, v80
	v_mfma_f32_16x16x32_bf16 v[92:95], v[160:163], v[112:115], 0
	v_exp_f32_e32 v84, v84
	ds_read_b128 v[234:237], v210 offset:47104
	s_waitcnt lgkmcnt(6)
	v_mfma_f32_16x16x32_bf16 v[32:35], v[164:167], v[242:245], v[32:35]
	v_exp_f32_e32 v81, v81
	v_mfma_f32_16x16x32_bf16 v[36:39], v[164:167], v[204:207], v[36:39]
	v_exp_f32_e32 v85, v85
	ds_read_b128 v[160:163], v201 offset:0
	s_waitcnt lgkmcnt(6)
	v_mfma_f32_16x16x32_bf16 v[92:95], v[168:171], v[116:119], v[92:95]
	v_exp_f32_e32 v82, v82
	v_mfma_f32_16x16x32_bf16 v[88:91], v[168:171], v[100:103], v[88:91]
	v_exp_f32_e32 v86, v86
	ds_read_b128 v[164:167], v209 offset:49152
	s_waitcnt lgkmcnt(6)
	v_mfma_f32_16x16x32_bf16 v[44:47], v[172:175], v[204:207], v[44:47]
	v_exp_f32_e32 v83, v83
	v_mfma_f32_16x16x32_bf16 v[40:43], v[172:175], v[242:245], v[40:43]
	v_exp_f32_e32 v87, v87
	ds_read_b128 v[168:171], v202 offset:0
	s_waitcnt lgkmcnt(6)
	v_mfma_f32_16x16x32_bf16 v[88:91], v[176:179], v[104:107], v[88:91]
	v_add_f32_e32 v220, v220, v80
	v_add_f32_e32 v221, v221, v84
	v_mfma_f32_16x16x32_bf16 v[92:95], v[176:179], v[120:123], v[92:95]
	v_add_f32_e32 v220, v220, v81
	ds_read_b128 v[172:175], v209 offset:51200
	s_waitcnt lgkmcnt(6)
	v_mfma_f32_16x16x32_bf16 v[48:51], v[180:183], v[242:245], v[48:51]
	v_add_f32_e32 v221, v221, v85
	v_add_f32_e32 v220, v220, v82
	v_mfma_f32_16x16x32_bf16 v[52:55], v[180:183], v[204:207], v[52:55]
	v_add_f32_e32 v221, v221, v86
	ds_read_b128 v[176:179], v203 offset:0
	s_waitcnt lgkmcnt(6)
	v_mfma_f32_16x16x32_bf16 v[92:95], v[230:233], v[124:127], v[92:95]
	v_add_f32_e32 v220, v220, v83
	v_add_f32_e32 v221, v221, v87
	v_mfma_f32_16x16x32_bf16 v[88:91], v[230:233], v[108:111], v[88:91]
	v_cvt_pk_bf16_f32 v218, v72, v73
	ds_read_b128 v[180:183], v209 offset:53248
	s_waitcnt lgkmcnt(6)
	v_mfma_f32_16x16x32_bf16 v[60:63], v[234:237], v[204:207], v[60:63]
	v_cvt_pk_bf16_f32 v219, v74, v75
	v_cvt_pk_bf16_f32 v240, v76, v77
	v_mfma_f32_16x16x32_bf16 v[56:59], v[234:237], v[242:245], v[56:59]
	v_cvt_pk_bf16_f32 v241, v78, v79
	ds_read_b128 v[230:233], v246 offset:0
	s_cmp_eq_u32 s100, 1
	s_cbranch_scc1 .Lattn_pa3
	s_setprio 1
	s_branch .Lattn_pb3

.Lattn_pb3:
	s_waitcnt lgkmcnt(6)
	v_mfma_f32_16x16x32_bf16 v[64:67], v[160:163], v[96:99], 0
	v_exp_f32_e32 v88, v88
	v_mfma_f32_16x16x32_bf16 v[68:71], v[160:163], v[112:115], 0
	v_exp_f32_e32 v92, v92
	ds_read_b128 v[234:237], v209 offset:55296
	s_add_u32 s8, s16, 0x3bc00380
	s_addc_u32 s9, s17, 0
	s_add_u32 s6, s15, 0x23a80000
	s_addc_u32 s7, s14, 0
	s_waitcnt lgkmcnt(6)
	v_mfma_f32_16x16x32_bf16 v[0:3], v[164:167], v[216:219], v[0:3]
	v_cvt_pk_bf16_f32 v242, v80, v81
	v_mfma_f32_16x16x32_bf16 v[4:7], v[164:167], v[238:241], v[4:7]
	v_exp_f32_e32 v89, v89
	ds_read_b128 v[160:163], v201 offset:4096
	s_waitcnt vmcnt(4)
	ds_write_b128 v225, v[136:139] offset:32768
	s_waitcnt lgkmcnt(7)
	v_mfma_f32_16x16x32_bf16 v[68:71], v[168:171], v[116:119], v[68:71]
	v_exp_f32_e32 v93, v93
	v_mfma_f32_16x16x32_bf16 v[64:67], v[168:171], v[100:103], v[64:67]
	v_cvt_pk_bf16_f32 v243, v82, v83
	ds_read_b128 v[164:167], v209 offset:57344
	ds_write_b128 v226, v[140:143] offset:32768
	s_waitcnt lgkmcnt(8)
	v_mfma_f32_16x16x32_bf16 v[12:15], v[172:175], v[238:241], v[12:15]
	v_exp_f32_e32 v90, v90
	v_mfma_f32_16x16x32_bf16 v[8:11], v[172:175], v[216:219], v[8:11]
	v_exp_f32_e32 v94, v94
	ds_read_b128 v[168:171], v202 offset:4096
	ds_write_b64 v227, v[148:149] offset:16384
	s_waitcnt lgkmcnt(9)
	v_mfma_f32_16x16x32_bf16 v[64:67], v[176:179], v[104:107], v[64:67]
	v_cvt_pk_bf16_f32 v204, v84, v85
	v_mfma_f32_16x16x32_bf16 v[68:71], v[176:179], v[120:123], v[68:71]
	v_exp_f32_e32 v91, v91
	ds_read_b128 v[172:175], v209 offset:59392
	ds_write_b64 v228, v[150:151] offset:16384
	s_waitcnt lgkmcnt(10)
	v_mfma_f32_16x16x32_bf16 v[16:19], v[180:183], v[216:219], v[16:19]
	v_exp_f32_e32 v95, v95
	v_mfma_f32_16x16x32_bf16 v[20:23], v[180:183], v[238:241], v[20:23]
	v_cvt_pk_bf16_f32 v205, v86, v87
	v_add_f32_e32 v220, v220, v88
	ds_read_b128 v[176:179], v203 offset:4096
	ds_write_b64 v229, v[144:145] offset:16384
	s_waitcnt lgkmcnt(11)
	v_mfma_f32_16x16x32_bf16 v[68:71], v[230:233], v[124:127], v[68:71]
	v_add_f32_e32 v221, v221, v92
	v_add_f32_e32 v220, v220, v89
	v_mfma_f32_16x16x32_bf16 v[64:67], v[230:233], v[108:111], v[64:67]
	v_add_f32_e32 v221, v221, v93
	v_cvt_pk_bf16_f32 v244, v88, v89
	ds_read_b128 v[180:183], v209 offset:61440
	ds_write_b64 v184, v[146:147] offset:16384
	s_waitcnt lgkmcnt(12)
	v_mfma_f32_16x16x32_bf16 v[28:31], v[234:237], v[238:241], v[28:31]
	v_cvt_pk_bf16_f32 v245, v90, v91
	v_cvt_pk_bf16_f32 v206, v92, v93
	v_mfma_f32_16x16x32_bf16 v[24:27], v[234:237], v[216:219], v[24:27]
	v_cvt_pk_bf16_f32 v207, v94, v95
	ds_read_b128 v[230:233], v246 offset:4096
	global_load_dwordx4 v[148:151], v198, s[8:9]
	s_waitcnt lgkmcnt(12)
	v_mfma_f32_16x16x32_bf16 v[72:75], v[160:163], v[96:99], 0
	v_add_f32_e32 v220, v220, v90
	v_add_f32_e32 v221, v221, v94
	v_mfma_f32_16x16x32_bf16 v[76:79], v[160:163], v[112:115], 0
	v_add_f32_e32 v220, v220, v91
	v_add_f32_e32 v221, v221, v95
	ds_read_b128 v[234:237], v209 offset:63488
	global_load_dwordx4 v[144:147], v199, s[8:9]
	s_waitcnt lgkmcnt(11)
	v_mfma_f32_16x16x32_bf16 v[32:35], v[164:167], v[216:219], v[32:35]
	v_add_f32_e32 v194, v194, v220
	v_add_f32_e32 v195, v195, v221
	v_mfma_f32_16x16x32_bf16 v[36:39], v[164:167], v[238:241], v[36:39]
	v_exp_f32_e32 v64, v64
	ds_read_b128 v[160:163], v201 offset:8192
	global_load_dwordx4 v[136:139], v196, s[6:7]
	s_waitcnt lgkmcnt(10)
	v_mfma_f32_16x16x32_bf16 v[76:79], v[168:171], v[116:119], v[76:79]
	v_exp_f32_e32 v68, v68
	v_mfma_f32_16x16x32_bf16 v[72:75], v[168:171], v[100:103], v[72:75]
	v_exp_f32_e32 v65, v65
	ds_read_b128 v[164:167], v210 offset:49152
	global_load_dwordx4 v[140:143], v197, s[6:7]
	s_waitcnt lgkmcnt(9)
	v_mfma_f32_16x16x32_bf16 v[44:47], v[172:175], v[238:241], v[44:47]
	v_exp_f32_e32 v69, v69
	v_mfma_f32_16x16x32_bf16 v[40:43], v[172:175], v[216:219], v[40:43]
	v_exp_f32_e32 v66, v66
	ds_read_b128 v[168:171], v202 offset:8192
	s_waitcnt lgkmcnt(8)
	v_mfma_f32_16x16x32_bf16 v[72:75], v[176:179], v[104:107], v[72:75]
	v_exp_f32_e32 v70, v70
	v_mfma_f32_16x16x32_bf16 v[76:79], v[176:179], v[120:123], v[76:79]
	v_exp_f32_e32 v67, v67
	ds_read_b128 v[172:175], v210 offset:51200
	s_waitcnt lgkmcnt(7)
	v_mfma_f32_16x16x32_bf16 v[48:51], v[180:183], v[216:219], v[48:51]
	v_exp_f32_e32 v71, v71
	v_mfma_f32_16x16x32_bf16 v[52:55], v[180:183], v[238:241], v[52:55]
	v_add_f32_e32 v220, v64, v65
	ds_read_b128 v[176:179], v203 offset:8192
	s_waitcnt lgkmcnt(6)
	v_mfma_f32_16x16x32_bf16 v[76:79], v[230:233], v[124:127], v[76:79]
	v_add_f32_e32 v221, v68, v69
	v_mfma_f32_16x16x32_bf16 v[72:75], v[230:233], v[108:111], v[72:75]
	v_add_f32_e32 v220, v220, v66
	ds_read_b128 v[180:183], v210 offset:53248
	s_waitcnt lgkmcnt(6)
	v_mfma_f32_16x16x32_bf16 v[60:63], v[234:237], v[238:241], v[60:63]
	v_add_f32_e32 v221, v221, v70
	v_add_f32_e32 v220, v220, v67
	v_mfma_f32_16x16x32_bf16 v[56:59], v[234:237], v[216:219], v[56:59]
	v_add_f32_e32 v221, v221, v71
	ds_read_b128 v[230:233], v246 offset:8192
	s_waitcnt lgkmcnt(6)
	v_mfma_f32_16x16x32_bf16 v[80:83], v[160:163], v[96:99], 0
	v_exp_f32_e32 v72, v72
	v_mfma_f32_16x16x32_bf16 v[84:87], v[160:163], v[112:115], 0
	v_exp_f32_e32 v76, v76
	ds_read_b128 v[234:237], v210 offset:55296
	s_waitcnt lgkmcnt(6)
	v_mfma_f32_16x16x32_bf16 v[0:3], v[164:167], v[242:245], v[0:3]
	v_exp_f32_e32 v73, v73
	v_mfma_f32_16x16x32_bf16 v[4:7], v[164:167], v[204:207], v[4:7]
	v_exp_f32_e32 v77, v77
	ds_read_b128 v[160:163], v201 offset:12288
	s_waitcnt lgkmcnt(6)
	v_mfma_f32_16x16x32_bf16 v[84:87], v[168:171], v[116:119], v[84:87]
	v_exp_f32_e32 v74, v74
	v_mfma_f32_16x16x32_bf16 v[80:83], v[168:171], v[100:103], v[80:83]
	v_exp_f32_e32 v78, v78
	ds_read_b128 v[164:167], v210 offset:57344
	s_waitcnt lgkmcnt(6)
	v_mfma_f32_16x16x32_bf16 v[12:15], v[172:175], v[204:207], v[12:15]
	v_exp_f32_e32 v75, v75
	v_mfma_f32_16x16x32_bf16 v[8:11], v[172:175], v[242:245], v[8:11]
	v_exp_f32_e32 v79, v79
	ds_read_b128 v[168:171], v202 offset:12288
	s_waitcnt lgkmcnt(6)
	v_mfma_f32_16x16x32_bf16 v[80:83], v[176:179], v[104:107], v[80:83]
	v_add_f32_e32 v220, v220, v72
	v_add_f32_e32 v221, v221, v76
	v_mfma_f32_16x16x32_bf16 v[84:87], v[176:179], v[120:123], v[84:87]
	v_add_f32_e32 v220, v220, v73
	ds_read_b128 v[172:175], v210 offset:59392
	s_add_u32 s10, s10, 0x200
	s_addc_u32 s11, s11, 0
	s_add_u32 s12, s12, 0x40000
	s_addc_u32 s13, s13, 0
	s_add_i32 s4, s4, 4
	s_cmpk_lt_u32 s4, 0x104
	s_cselect_b64 s[6:7], -1, 0
	s_and_b64 s[6:7], s[0:1], s[6:7]
	s_and_b64 vcc, exec, s[6:7]
	s_waitcnt lgkmcnt(6)
	v_mfma_f32_16x16x32_bf16 v[16:19], v[180:183], v[242:245], v[16:19]
	v_add_f32_e32 v221, v221, v77
	v_add_f32_e32 v220, v220, v74
	v_mfma_f32_16x16x32_bf16 v[20:23], v[180:183], v[204:207], v[20:23]
	v_add_f32_e32 v221, v221, v78
	ds_read_b128 v[176:179], v203 offset:12288
	s_waitcnt lgkmcnt(6)
	v_mfma_f32_16x16x32_bf16 v[84:87], v[230:233], v[124:127], v[84:87]
	v_add_f32_e32 v220, v220, v75
	v_add_f32_e32 v221, v221, v79
	v_mfma_f32_16x16x32_bf16 v[80:83], v[230:233], v[108:111], v[80:83]
	v_cvt_pk_bf16_f32 v216, v64, v65
	ds_read_b128 v[180:183], v210 offset:61440
	s_waitcnt lgkmcnt(6)
	v_mfma_f32_16x16x32_bf16 v[28:31], v[234:237], v[204:207], v[28:31]
	v_cvt_pk_bf16_f32 v217, v66, v67
	v_cvt_pk_bf16_f32 v238, v68, v69
	v_mfma_f32_16x16x32_bf16 v[24:27], v[234:237], v[242:245], v[24:27]
	v_cvt_pk_bf16_f32 v239, v70, v71
	ds_read_b128 v[230:233], v246 offset:12288
	s_waitcnt lgkmcnt(6)
	v_mfma_f32_16x16x32_bf16 v[88:91], v[160:163], v[96:99], 0
	v_exp_f32_e32 v80, v80
	v_mfma_f32_16x16x32_bf16 v[92:95], v[160:163], v[112:115], 0
	v_exp_f32_e32 v84, v84
	ds_read_b128 v[234:237], v210 offset:63488
	s_waitcnt lgkmcnt(6)
	v_mfma_f32_16x16x32_bf16 v[32:35], v[164:167], v[242:245], v[32:35]
	v_exp_f32_e32 v81, v81
	v_mfma_f32_16x16x32_bf16 v[36:39], v[164:167], v[204:207], v[36:39]
	v_exp_f32_e32 v85, v85
	s_waitcnt lgkmcnt(5)
	v_mfma_f32_16x16x32_bf16 v[92:95], v[168:171], v[116:119], v[92:95]
	v_exp_f32_e32 v82, v82
	v_mfma_f32_16x16x32_bf16 v[88:91], v[168:171], v[100:103], v[88:91]
	v_exp_f32_e32 v86, v86
	s_waitcnt lgkmcnt(4)
	v_mfma_f32_16x16x32_bf16 v[44:47], v[172:175], v[204:207], v[44:47]
	v_exp_f32_e32 v83, v83
	v_mfma_f32_16x16x32_bf16 v[40:43], v[172:175], v[242:245], v[40:43]
	v_exp_f32_e32 v87, v87
	s_waitcnt lgkmcnt(3)
	v_mfma_f32_16x16x32_bf16 v[88:91], v[176:179], v[104:107], v[88:91]
	v_add_f32_e32 v220, v220, v80
	v_add_f32_e32 v221, v221, v84
	v_mfma_f32_16x16x32_bf16 v[92:95], v[176:179], v[120:123], v[92:95]
	v_add_f32_e32 v220, v220, v81
	s_waitcnt lgkmcnt(2)
	v_mfma_f32_16x16x32_bf16 v[48:51], v[180:183], v[242:245], v[48:51]
	v_add_f32_e32 v221, v221, v85
	v_add_f32_e32 v220, v220, v82
	v_mfma_f32_16x16x32_bf16 v[52:55], v[180:183], v[204:207], v[52:55]
	v_add_f32_e32 v221, v221, v86
	s_waitcnt lgkmcnt(1)
	v_mfma_f32_16x16x32_bf16 v[92:95], v[230:233], v[124:127], v[92:95]
	v_add_f32_e32 v220, v220, v83
	v_add_f32_e32 v221, v221, v87
	v_mfma_f32_16x16x32_bf16 v[88:91], v[230:233], v[108:111], v[88:91]
	v_cvt_pk_bf16_f32 v218, v72, v73
	s_waitcnt lgkmcnt(0)
	v_mfma_f32_16x16x32_bf16 v[60:63], v[234:237], v[204:207], v[60:63]
	v_cvt_pk_bf16_f32 v219, v74, v75
	v_cvt_pk_bf16_f32 v240, v76, v77
	v_mfma_f32_16x16x32_bf16 v[56:59], v[234:237], v[242:245], v[56:59]
	v_cvt_pk_bf16_f32 v241, v78, v79
	s_cbranch_vccnz .LBB0_734
	s_setprio 0
	s_waitcnt vmcnt(0)
	s_nop 7
	s_nop 7
	ds_swizzle_b32 v64, v194 offset:swizzle(SWAP,16)
	s_waitcnt lgkmcnt(0)
	v_add_f32_e32 v194, v194, v64
	v_mov_b32_e32 v65, v194
	s_nop 1
	v_permlane32_swap_b32_e32 v194, v65
	v_add_f32_e32 v194, v194, v65
	s_nop 0
	v_rcp_f32_e32 v66, v194
	ds_swizzle_b32 v64, v195 offset:swizzle(SWAP,16)
	s_waitcnt lgkmcnt(0)
	v_add_f32_e32 v195, v195, v64
	v_mov_b32_e32 v65, v195
	s_nop 1
	v_permlane32_swap_b32_e32 v195, v65
	v_add_f32_e32 v195, v195, v65
	s_nop 0
	v_rcp_f32_e32 v67, v195
	v_readlane_b32 s100, v250, 8
	v_mbcnt_lo_u32_b32 v68, -1, 0
	v_mbcnt_hi_u32_b32 v68, -1, v68
	v_and_b32_e32 v69, 15, v68
	v_lshrrev_b32_e32 v70, 4, v68
	s_lshr_b32 s101, s100, 1
	v_add_u32_e32 v69, s101, v69
	v_lshlrev_b32_e32 v69, 12, v69
	v_and_b32_e32 v71, 1, v70
	v_lshlrev_b32_e32 v71, 5, v71
	v_and_b32_e32 v70, 2, v70
	v_lshl_add_u32 v71, v70, 3, v71
	v_add_u32_e32 v70, v69, v71
	v_add_u32_e32 v71, 0x10000, v70
	v_mul_f32_e32 v0, v0, v66
	v_mul_f32_e32 v1, v1, v66
	v_mul_f32_e32 v2, v2, v66
	v_mul_f32_e32 v3, v3, v66
	v_mul_f32_e32 v8, v8, v66
	v_mul_f32_e32 v9, v9, v66
	v_mul_f32_e32 v10, v10, v66
	v_mul_f32_e32 v11, v11, v66
	v_cvt_pk_bf16_f32 v72, v0, v1
	v_cvt_pk_bf16_f32 v73, v2, v3
	v_cvt_pk_bf16_f32 v74, v8, v9
	v_cvt_pk_bf16_f32 v75, v10, v11
	s_nop 1
	v_permlane16_swap_b32_e32 v72, v74
	v_permlane16_swap_b32_e32 v73, v75
	s_nop 1
	global_store_dwordx4 v70, v[72:75], s[58:59] offset:0
	v_mul_f32_e32 v16, v16, v66
	v_mul_f32_e32 v17, v17, v66
	v_mul_f32_e32 v18, v18, v66
	v_mul_f32_e32 v19, v19, v66
	v_mul_f32_e32 v24, v24, v66
	v_mul_f32_e32 v25, v25, v66
	v_mul_f32_e32 v26, v26, v66
	v_mul_f32_e32 v27, v27, v66
	v_cvt_pk_bf16_f32 v76, v16, v17
	v_cvt_pk_bf16_f32 v77, v18, v19
	v_cvt_pk_bf16_f32 v78, v24, v25
	v_cvt_pk_bf16_f32 v79, v26, v27
	s_nop 1
	v_permlane16_swap_b32_e32 v76, v78
	v_permlane16_swap_b32_e32 v77, v79
	s_nop 1
	global_store_dwordx4 v70, v[76:79], s[58:59] offset:64
	v_mul_f32_e32 v32, v32, v66
	v_mul_f32_e32 v33, v33, v66
	v_mul_f32_e32 v34, v34, v66
	v_mul_f32_e32 v35, v35, v66
	v_mul_f32_e32 v40, v40, v66
	v_mul_f32_e32 v41, v41, v66
	v_mul_f32_e32 v42, v42, v66
	v_mul_f32_e32 v43, v43, v66
	v_cvt_pk_bf16_f32 v80, v32, v33
	v_cvt_pk_bf16_f32 v81, v34, v35
	v_cvt_pk_bf16_f32 v82, v40, v41
	v_cvt_pk_bf16_f32 v83, v42, v43
	s_nop 1
	v_permlane16_swap_b32_e32 v80, v82
	v_permlane16_swap_b32_e32 v81, v83
	s_nop 1
	global_store_dwordx4 v70, v[80:83], s[58:59] offset:128
	v_mul_f32_e32 v48, v48, v66
	v_mul_f32_e32 v49, v49, v66
	v_mul_f32_e32 v50, v50, v66
	v_mul_f32_e32 v51, v51, v66
	v_mul_f32_e32 v56, v56, v66
	v_mul_f32_e32 v57, v57, v66
	v_mul_f32_e32 v58, v58, v66
	v_mul_f32_e32 v59, v59, v66
	v_cvt_pk_bf16_f32 v84, v48, v49
	v_cvt_pk_bf16_f32 v85, v50, v51
	v_cvt_pk_bf16_f32 v86, v56, v57
	v_cvt_pk_bf16_f32 v87, v58, v59
	s_nop 1
	v_permlane16_swap_b32_e32 v84, v86
	v_permlane16_swap_b32_e32 v85, v87
	s_nop 1
	global_store_dwordx4 v70, v[84:87], s[58:59] offset:192
	v_mul_f32_e32 v4, v4, v67
	v_mul_f32_e32 v5, v5, v67
	v_mul_f32_e32 v6, v6, v67
	v_mul_f32_e32 v7, v7, v67
	v_mul_f32_e32 v12, v12, v67
	v_mul_f32_e32 v13, v13, v67
	v_mul_f32_e32 v14, v14, v67
	v_mul_f32_e32 v15, v15, v67
	v_cvt_pk_bf16_f32 v88, v4, v5
	v_cvt_pk_bf16_f32 v89, v6, v7
	v_cvt_pk_bf16_f32 v90, v12, v13
	v_cvt_pk_bf16_f32 v91, v14, v15
	s_nop 1
	v_permlane16_swap_b32_e32 v88, v90
	v_permlane16_swap_b32_e32 v89, v91
	s_nop 1
	global_store_dwordx4 v71, v[88:91], s[58:59] offset:0
	v_mul_f32_e32 v20, v20, v67
	v_mul_f32_e32 v21, v21, v67
	v_mul_f32_e32 v22, v22, v67
	v_mul_f32_e32 v23, v23, v67
	v_mul_f32_e32 v28, v28, v67
	v_mul_f32_e32 v29, v29, v67
	v_mul_f32_e32 v30, v30, v67
	v_mul_f32_e32 v31, v31, v67
	v_cvt_pk_bf16_f32 v92, v20, v21
	v_cvt_pk_bf16_f32 v93, v22, v23
	v_cvt_pk_bf16_f32 v94, v28, v29
	v_cvt_pk_bf16_f32 v95, v30, v31
	s_nop 1
	v_permlane16_swap_b32_e32 v92, v94
	v_permlane16_swap_b32_e32 v93, v95
	s_nop 1
	global_store_dwordx4 v71, v[92:95], s[58:59] offset:64
	v_mul_f32_e32 v36, v36, v67
	v_mul_f32_e32 v37, v37, v67
	v_mul_f32_e32 v38, v38, v67
	v_mul_f32_e32 v39, v39, v67
	v_mul_f32_e32 v44, v44, v67
	v_mul_f32_e32 v45, v45, v67
	v_mul_f32_e32 v46, v46, v67
	v_mul_f32_e32 v47, v47, v67
	v_cvt_pk_bf16_f32 v72, v36, v37
	v_cvt_pk_bf16_f32 v73, v38, v39
	v_cvt_pk_bf16_f32 v74, v44, v45
	v_cvt_pk_bf16_f32 v75, v46, v47
	s_nop 1
	v_permlane16_swap_b32_e32 v72, v74
	v_permlane16_swap_b32_e32 v73, v75
	s_nop 1
	global_store_dwordx4 v71, v[72:75], s[58:59] offset:128
	v_mul_f32_e32 v52, v52, v67
	v_mul_f32_e32 v53, v53, v67
	v_mul_f32_e32 v54, v54, v67
	v_mul_f32_e32 v55, v55, v67
	v_mul_f32_e32 v60, v60, v67
	v_mul_f32_e32 v61, v61, v67
	v_mul_f32_e32 v62, v62, v67
	v_mul_f32_e32 v63, v63, v67
	v_cvt_pk_bf16_f32 v76, v52, v53
	v_cvt_pk_bf16_f32 v77, v54, v55
	v_cvt_pk_bf16_f32 v78, v60, v61
	v_cvt_pk_bf16_f32 v79, v62, v63
	s_nop 1
	v_permlane16_swap_b32_e32 v76, v78
	v_permlane16_swap_b32_e32 v77, v79
	s_nop 1
	global_store_dwordx4 v71, v[76:79], s[58:59] offset:192
	s_barrier
